# three more uniform mask negations (outside the P4 chunk loop) moved from VALU cndmask+cmp_ne to s_andn2_b64
# baseline (speedup 1.0000x reference)
.LBB0_423:
	v_or_b32_e32 v80, s70, v82
	v_mov_b64_e32 v[2:3], s[2:3]
	v_mad_i64_i32 v[2:3], s[48:49], v80, s86, v[2:3]
	s_lshl_b32 s50, s71, 7
	v_lshl_add_u64 v[2:3], v[2:3], 0, s[50:51]
	v_lshl_add_u64 v[2:3], v[2:3], 0, v[66:67]
	global_load_dwordx4 v[6:9], v[2:3], off offset:512
	s_nop 0
	global_load_dwordx4 v[2:5], v[2:3], off offset:576
	s_add_i32 s72, s72, s81
	v_lshl_add_u32 v11, s69, 11, v71
	s_lshl_b32 s62, s71, 6
	s_andn2_b64 s[48:49], exec, s[58:59]
	v_lshl_add_u32 v10, s72, 6, v11
	s_mov_b64 s[60:61], 0
	v_mov_b32_e32 v34, 0
	v_mov_b32_e32 v35, 0
	v_mov_b32_e32 v36, 0
	v_mov_b32_e32 v37, 0
	v_mov_b32_e32 v38, 0
	v_mov_b32_e32 v39, 0
	v_mov_b32_e32 v40, 0
	v_mov_b32_e32 v41, 0
	v_mov_b32_e32 v42, 0
	v_mov_b32_e32 v43, 0
	v_mov_b32_e32 v44, 0
	v_mov_b32_e32 v45, 0
	v_mov_b32_e32 v46, 0
	v_mov_b32_e32 v47, 0
	v_mov_b32_e32 v48, 0
	v_mov_b32_e32 v49, 0
	v_mov_b32_e32 v50, 0
	v_mov_b32_e32 v51, 0
	v_mov_b32_e32 v52, 0
	v_mov_b32_e32 v53, 0
	v_mov_b32_e32 v54, 0
	v_mov_b32_e32 v55, 0
	v_mov_b32_e32 v56, 0
	v_mov_b32_e32 v57, 0
	v_mov_b32_e32 v58, 0
	v_mov_b32_e32 v59, 0
	v_mov_b32_e32 v60, 0
	v_mov_b32_e32 v61, 0
	v_mov_b32_e32 v62, 0
	v_mov_b32_e32 v63, 0
	v_mov_b32_e32 v64, 0
	v_mov_b32_e32 v65, 0
	s_andn2_b64 vcc, exec, s[58:59]
	s_cbranch_vccnz .LBB0_439
	v_mov_b64_e32 v[12:13], s[2:3]
	v_mad_i64_i32 v[12:13], s[64:65], v10, s86, v[12:13]
	s_lshl_b32 s50, s62, 1
	v_lshl_add_u64 v[12:13], v[12:13], 0, s[50:51]
	v_lshl_add_u64 v[12:13], v[12:13], 0, v[66:67]
	v_add_co_u32_e32 v14, vcc, 0x30000, v12
	v_addc_co_u32_e32 v15, vcc, 0, v13, vcc
	v_add_co_u32_e32 v16, vcc, 0xc0000, v12
	v_addc_co_u32_e32 v17, vcc, 0, v13, vcc
	v_add_co_u32_e32 v18, vcc, 0xf0000, v12
	v_addc_co_u32_e32 v19, vcc, 0, v13, vcc
	v_add_co_u32_e32 v20, vcc, 0x180000, v12
	v_addc_co_u32_e32 v21, vcc, 0, v13, vcc
	v_add_co_u32_e32 v22, vcc, 0x1b0000, v12
	v_addc_co_u32_e32 v23, vcc, 0, v13, vcc
	v_add_co_u32_e32 v24, vcc, 0x240000, v12
	v_addc_co_u32_e32 v25, vcc, 0, v13, vcc
	v_add_co_u32_e32 v26, vcc, 0x270000, v12
	v_addc_co_u32_e32 v27, vcc, 0, v13, vcc
	global_load_dwordx4 v[160:163], v[12:13], off offset:1024
	global_load_dwordx4 v[164:167], v[14:15], off offset:1024
	global_load_dwordx4 v[168:171], v[16:17], off offset:1024
	global_load_dwordx4 v[172:175], v[18:19], off offset:1024
	global_load_dwordx4 v[176:179], v[20:21], off offset:1024
	global_load_dwordx4 v[180:183], v[22:23], off offset:1024
	global_load_dwordx4 v[184:187], v[24:25], off offset:1024
	global_load_dwordx4 v[188:191], v[26:27], off offset:1024
	global_load_dwordx4 v[192:195], v[12:13], off offset:1088
	global_load_dwordx4 v[196:199], v[14:15], off offset:1088
	global_load_dwordx4 v[200:203], v[16:17], off offset:1088
	global_load_dwordx4 v[204:207], v[18:19], off offset:1088
	global_load_dwordx4 v[208:211], v[20:21], off offset:1088
	global_load_dwordx4 v[214:217], v[22:23], off offset:1088
	global_load_dwordx4 v[218:221], v[24:25], off offset:1088
	global_load_dwordx4 v[222:225], v[26:27], off offset:1088
	s_and_b64 s[60:61], s[56:57], exec
